# one static s_setprio 1 for waves 4-7 across the attention part of the attention/FFT1 phase (reset to 0 at its end); timing-only, bit-identical
# baseline (speedup 1.0000x reference)
.LBB0_353:
	s_setprio 0
	s_waitcnt lgkmcnt(0)
	s_barrier

.LBB0_383:
	s_andn2_b64 vcc, exec, s[2:3]
	s_cbranch_vccnz .LBB0_354
	v_readfirstlane_b32 s101, v0
	s_lshr_b32 s101, s101, 8
	s_cmp_lg_u32 s101, 0
	s_mov_b32 s101, 0
	s_cbranch_scc0 .Lattn_prio_done
	s_setprio 1
.Lattn_prio_done:
	v_mov_b32_e32 v2, v0
	s_mov_b32 s18, s37
	s_mov_b64 s[2:3], 0
	v_readlane_b32 s19, v253, 8
	s_and_b32 s6, s18, 7
	s_cmp_lg_u32 s6, 0
	s_cbranch_scc0 .LBB0_386
	s_cmpk_gt_i32 s19, 0x1ff
	s_cbranch_scc1 .LBB0_353
	s_branch .LBB0_387
